# speedup vs baseline: 1.0013x; 1.0013x over previous
.LBB1_68:
	s_bfe_u32 s82, s8, 0x80010
	s_and_b32 s82, s82, 7
	s_mov_b32 s77, s82
	s_lshl_b32 s78, s82, 8
	s_lshl_b32 s79, s82, 7
	s_add_u32 s80, s52, s79
	s_addc_u32 s81, s53, 0
	v_mov_b32_e32 v2, v0
	s_bfe_u32 s21, s8, 0x80010
	s_lshl_b32 s13, s21, 7
	v_lshrrev_b32_e32 v3, 2, v2
	v_and_b32_e32 v3, 0xffffe0, v3
	v_add_u32_e32 v3, s13, v3
	v_lshrrev_b32_e32 v4, 3, v2
	v_and_or_b32 v3, v4, 7, v3
	s_movk_i32 s6, 0x300
	v_mul_lo_u32 v3, v3, s6
	v_lshlrev_b32_e32 v2, 2, v2
	v_and_or_b32 v2, v2, 28, v3
	v_lshlrev_b32_e32 v2, 2, v2
	v_add_u32_e32 v2, s78, v2
	v_mov_b32_e32 v3, 0
	v_lshl_add_u64 v[4:5], s[2:3], 0, v[2:3]
	global_load_dwordx4 v[26:29], v2, s[2:3] nt
	global_load_dwordx4 v[18:21], v2, s[2:3] offset:128 nt
	global_load_dwordx4 v[114:117], v2, s[2:3] offset:256 nt
	global_load_dwordx4 v[118:121], v2, s[2:3] offset:384 nt
	s_movk_i32 s2, 0x6000
	v_add_co_u32_e32 v2, vcc, s2, v4
	s_mov_b32 s2, 0xc000
	s_nop 0
	v_addc_co_u32_e32 v3, vcc, 0, v5, vcc
	global_load_dwordx4 v[30:33], v[2:3], off nt
	global_load_dwordx4 v[14:17], v[2:3], off offset:128 nt
	global_load_dwordx4 v[122:125], v[2:3], off offset:256 nt
	global_load_dwordx4 v[126:129], v[2:3], off offset:384 nt
	v_add_co_u32_e32 v2, vcc, s2, v4
	s_nop 1
	v_addc_co_u32_e32 v3, vcc, 0, v5, vcc
	v_add_co_u32_e32 v36, vcc, 0x12000, v4
	global_load_dwordx4 v[22:25], v[2:3], off nt
	global_load_dwordx4 v[6:9], v[2:3], off offset:128 nt
	global_load_dwordx4 v[130:133], v[2:3], off offset:256 nt
	global_load_dwordx4 v[134:137], v[2:3], off offset:384 nt
	v_addc_co_u32_e32 v37, vcc, 0, v5, vcc
	global_load_dwordx4 v[10:13], v[36:37], off nt
	global_load_dwordx4 v[138:141], v[36:37], off offset:256 nt
	global_load_dwordx4 v[142:145], v[36:37], off offset:384 nt
	global_load_dwordx4 v[2:5], v[36:37], off offset:128 nt
	v_cmp_gt_u32_e32 vcc, 64, v0
	s_and_b32 s12, s8, 0xffff
	s_and_saveexec_b64 s[6:7], vcc
	s_cbranch_execz .LBB1_78
	s_cmp_eq_u32 s9, 8
	s_cselect_b64 vcc, -1, 0
	s_add_i32 s2, s12, 0xffffe800
	v_mov_b32_e32 v37, 0x24000
	v_add_u32_e32 v35, s2, v34
	v_add_u32_e32 v38, 64, v35
	v_cndmask_b32_e32 v36, 0, v35, vcc
	v_lshl_add_u32 v37, v34, 2, v37
	v_cndmask_b32_e32 v38, 0, v38, vcc
	ds_write2st64_b32 v37, v36, v38 offset1:1
	v_add_u32_e32 v36, 0x80, v35
	v_add_u32_e32 v35, 0xc0, v35
	v_cndmask_b32_e32 v36, 0, v36, vcc
	v_cndmask_b32_e32 v35, 0, v35, vcc
	s_andn2_b64 vcc, exec, s[0:1]
	ds_write2st64_b32 v37, v36, v35 offset0:2 offset1:3
	s_cbranch_vccnz .LBB1_78
	v_mov_b32_e32 v35, 0x20000
	v_lshl_add_u32 v44, v34, 3, v35
	ds_read2st64_b64 v[36:39], v44 offset1:1
	ds_read2st64_b64 v[40:43], v44 offset0:2 offset1:3
	v_mov_b32_e32 v61, 0x100
	v_mov_b32_e32 v69, 0x1000
	v_mov_b32_e32 v77, 0x10000
	s_waitcnt lgkmcnt(1)
	v_cmp_eq_u32_e64 s[2:3], s9, v38
	v_cmp_eq_u32_e32 vcc, s9, v36
	v_cmp_eq_u32_e64 s[0:1], s9, v37
	v_cndmask_b32_e64 v45, 0, 2, s[2:3]
	v_cmp_eq_u32_e64 s[2:3], s9, v39
	ds_read2st64_b64 v[36:39], v44 offset0:4 offset1:5
	v_mov_b32_e32 v84, 0x100000
	v_cndmask_b32_e64 v46, 0, 2, s[2:3]
	s_waitcnt lgkmcnt(1)
	v_cmp_eq_u32_e64 s[2:3], s9, v40
	v_mov_b32_e32 v92, 0x1000000
	v_bfrev_b32_e32 v100, 8
	v_cndmask_b32_e64 v47, 0, 4, s[2:3]
	v_cmp_eq_u32_e64 s[2:3], s9, v41
	s_or_b64 s[0:1], s[0:1], vcc
	s_cmp_lt_u32 s8, 0x1000000
	v_cndmask_b32_e64 v48, 0, 4, s[2:3]
	v_cmp_eq_u32_e64 s[2:3], s9, v42
	s_nop 1
	v_cndmask_b32_e64 v49, 0, 8, s[2:3]
	v_cmp_eq_u32_e64 s[2:3], s9, v43
	ds_read2st64_b64 v[40:43], v44 offset0:6 offset1:7
	s_nop 0
	v_cndmask_b32_e64 v52, 0, 8, s[2:3]
	s_waitcnt lgkmcnt(1)
	v_cmp_eq_u32_e64 s[2:3], s9, v36
	s_nop 1
	v_cndmask_b32_e64 v53, 0, 16, s[2:3]
	v_cmp_eq_u32_e64 s[2:3], s9, v37
	s_nop 1
	v_cndmask_b32_e64 v54, 0, 16, s[2:3]
	v_cmp_eq_u32_e64 s[2:3], s9, v38
	s_nop 1
	v_cndmask_b32_e64 v55, 0, 32, s[2:3]
	v_cmp_eq_u32_e64 s[2:3], s9, v39
	ds_read2st64_b64 v[36:39], v44 offset0:8 offset1:9
	s_nop 0
	v_cndmask_b32_e64 v56, 0, 32, s[2:3]
	s_waitcnt lgkmcnt(1)
	v_cmp_eq_u32_e64 s[2:3], s9, v40
	v_mov_b32_e32 v40, 0x80
	s_nop 0
	v_cndmask_b32_e64 v57, 0, 64, s[2:3]
	v_cmp_eq_u32_e64 s[2:3], s9, v41
	s_nop 1
	v_cndmask_b32_e64 v58, 0, 64, s[2:3]
	v_cmp_eq_u32_e64 s[2:3], s9, v42
	s_nop 1
	v_cndmask_b32_e64 v59, 0, v40, s[2:3]
	v_cmp_eq_u32_e64 s[2:3], s9, v43
	s_nop 1
	v_cndmask_b32_e64 v60, 0, v40, s[2:3]
	ds_read2st64_b64 v[40:43], v44 offset0:10 offset1:11
	s_waitcnt lgkmcnt(1)
	v_cmp_eq_u32_e64 s[2:3], s9, v36
	v_mov_b32_e32 v36, 0x200
	s_nop 0
	v_cndmask_b32_e64 v62, 0, v61, s[2:3]
	v_cmp_eq_u32_e64 s[2:3], s9, v37
	s_nop 1
	v_cndmask_b32_e64 v61, 0, v61, s[2:3]
	v_cmp_eq_u32_e64 s[2:3], s9, v38
	s_nop 1
	v_cndmask_b32_e64 v63, 0, v36, s[2:3]
	v_cmp_eq_u32_e64 s[2:3], s9, v39
	s_nop 1
	v_cndmask_b32_e64 v64, 0, v36, s[2:3]
	v_mov_b32_e32 v36, 0x400
	s_waitcnt lgkmcnt(0)
	v_cmp_eq_u32_e64 s[2:3], s9, v40
	v_mov_b32_e32 v40, 0x800
	s_nop 0
	v_cndmask_b32_e64 v65, 0, v36, s[2:3]
	v_cmp_eq_u32_e64 s[2:3], s9, v41
	s_nop 1
	v_cndmask_b32_e64 v66, 0, v36, s[2:3]
	ds_read2st64_b64 v[36:39], v44 offset0:12 offset1:13
	v_cmp_eq_u32_e64 s[2:3], s9, v42
	s_nop 1
	v_cndmask_b32_e64 v67, 0, v40, s[2:3]
	v_cmp_eq_u32_e64 s[2:3], s9, v43
	s_nop 1
	v_cndmask_b32_e64 v68, 0, v40, s[2:3]
	ds_read2st64_b64 v[40:43], v44 offset0:14 offset1:15
	s_waitcnt lgkmcnt(1)
	v_cmp_eq_u32_e64 s[2:3], s9, v36
	v_mov_b32_e32 v36, 0x2000
	s_nop 0
	v_cndmask_b32_e64 v70, 0, v69, s[2:3]
	v_cmp_eq_u32_e64 s[2:3], s9, v37
	s_nop 1
	v_cndmask_b32_e64 v69, 0, v69, s[2:3]
	v_cmp_eq_u32_e64 s[2:3], s9, v38
	s_nop 1
	v_cndmask_b32_e64 v71, 0, v36, s[2:3]
	v_cmp_eq_u32_e64 s[2:3], s9, v39
	s_nop 1
	v_cndmask_b32_e64 v72, 0, v36, s[2:3]
	v_mov_b32_e32 v36, 0x4000
	s_waitcnt lgkmcnt(0)
	v_cmp_eq_u32_e64 s[2:3], s9, v40
	v_mov_b32_e32 v40, 0x8000
	s_nop 0
	v_cndmask_b32_e64 v73, 0, v36, s[2:3]
	v_cmp_eq_u32_e64 s[2:3], s9, v41
	s_nop 1
	v_cndmask_b32_e64 v74, 0, v36, s[2:3]
	ds_read2st64_b64 v[36:39], v44 offset0:16 offset1:17
	v_cmp_eq_u32_e64 s[2:3], s9, v42
	s_nop 1
	v_cndmask_b32_e64 v75, 0, v40, s[2:3]
	v_cmp_eq_u32_e64 s[2:3], s9, v43
	s_nop 1
	v_cndmask_b32_e64 v76, 0, v40, s[2:3]
	ds_read2st64_b64 v[40:43], v44 offset0:18 offset1:19
	s_waitcnt lgkmcnt(1)
	v_cmp_eq_u32_e64 s[2:3], s9, v36
	v_mov_b32_e32 v36, 0x40000
	s_nop 0
	v_cndmask_b32_e64 v78, 0, v77, s[2:3]
	v_cmp_eq_u32_e64 s[2:3], s9, v37
	s_nop 1
	v_cndmask_b32_e64 v77, 0, v77, s[2:3]
	v_cmp_eq_u32_e64 s[2:3], s9, v38
	s_nop 1
	v_cndmask_b32_e64 v79, 0, v35, s[2:3]
	v_cmp_eq_u32_e64 s[2:3], s9, v39
	s_nop 1
	v_cndmask_b32_e64 v35, 0, v35, s[2:3]
	s_waitcnt lgkmcnt(0)
	v_cmp_eq_u32_e64 s[2:3], s9, v40
	v_mov_b32_e32 v40, 0x80000
	s_nop 0
	v_cndmask_b32_e64 v80, 0, v36, s[2:3]
	v_cmp_eq_u32_e64 s[2:3], s9, v41
	s_nop 1
	v_cndmask_b32_e64 v81, 0, v36, s[2:3]
	ds_read2st64_b64 v[36:39], v44 offset0:20 offset1:21
	v_cmp_eq_u32_e64 s[2:3], s9, v42
	s_nop 1
	v_cndmask_b32_e64 v82, 0, v40, s[2:3]
	v_cmp_eq_u32_e64 s[2:3], s9, v43
	s_nop 1
	v_cndmask_b32_e64 v83, 0, v40, s[2:3]
	ds_read2st64_b64 v[40:43], v44 offset0:22 offset1:23
	s_waitcnt lgkmcnt(1)
	v_cmp_eq_u32_e64 s[2:3], s9, v36
	v_mov_b32_e32 v36, 0x200000
	s_nop 0
	v_cndmask_b32_e64 v85, 0, v84, s[2:3]
	v_cmp_eq_u32_e64 s[2:3], s9, v37
	s_nop 1
	v_cndmask_b32_e64 v84, 0, v84, s[2:3]
	v_cmp_eq_u32_e64 s[2:3], s9, v38
	s_nop 1
	v_cndmask_b32_e64 v86, 0, v36, s[2:3]
	v_cmp_eq_u32_e64 s[2:3], s9, v39
	s_nop 1
	v_cndmask_b32_e64 v87, 0, v36, s[2:3]
	v_mov_b32_e32 v36, 0x400000
	s_waitcnt lgkmcnt(0)
	v_cmp_eq_u32_e64 s[2:3], s9, v40
	v_mov_b32_e32 v40, 0x800000
	s_nop 0
	v_cndmask_b32_e64 v88, 0, v36, s[2:3]
	v_cmp_eq_u32_e64 s[2:3], s9, v41
	s_nop 1
	v_cndmask_b32_e64 v89, 0, v36, s[2:3]
	ds_read2st64_b64 v[36:39], v44 offset0:24 offset1:25
	v_cmp_eq_u32_e64 s[2:3], s9, v42
	s_nop 1
	v_cndmask_b32_e64 v90, 0, v40, s[2:3]
	v_cmp_eq_u32_e64 s[2:3], s9, v43
	s_nop 1
	v_cndmask_b32_e64 v91, 0, v40, s[2:3]
	ds_read2st64_b64 v[40:43], v44 offset0:26 offset1:27
	s_waitcnt lgkmcnt(1)
	v_cmp_eq_u32_e64 s[2:3], s9, v36
	v_bfrev_b32_e32 v36, 64
	s_nop 0
	v_cndmask_b32_e64 v93, 0, v92, s[2:3]
	v_cmp_eq_u32_e64 s[2:3], s9, v37
	s_nop 1
	v_cndmask_b32_e64 v92, 0, v92, s[2:3]
	v_cmp_eq_u32_e64 s[2:3], s9, v38
	s_nop 1
	v_cndmask_b32_e64 v94, 0, v36, s[2:3]
	v_cmp_eq_u32_e64 s[2:3], s9, v39
	s_nop 1
	v_cndmask_b32_e64 v95, 0, v36, s[2:3]
	v_bfrev_b32_e32 v36, 32
	s_waitcnt lgkmcnt(0)
	v_cmp_eq_u32_e64 s[2:3], s9, v40
	v_bfrev_b32_e32 v40, 16
	s_nop 0
	v_cndmask_b32_e64 v96, 0, v36, s[2:3]
	v_cmp_eq_u32_e64 s[2:3], s9, v41
	s_nop 1
	v_cndmask_b32_e64 v97, 0, v36, s[2:3]
	ds_read2st64_b64 v[36:39], v44 offset0:28 offset1:29
	v_cmp_eq_u32_e64 s[2:3], s9, v42
	s_nop 1
	v_cndmask_b32_e64 v98, 0, v40, s[2:3]
	v_cmp_eq_u32_e64 s[2:3], s9, v43
	s_nop 1
	v_cndmask_b32_e64 v99, 0, v40, s[2:3]
	ds_read2st64_b64 v[40:43], v44 offset0:30 offset1:31
	s_waitcnt lgkmcnt(1)
	v_cmp_eq_u32_e64 s[2:3], s9, v36
	v_bfrev_b32_e32 v44, 4
	s_nop 0
	v_cndmask_b32_e64 v36, 0, v100, s[2:3]
	v_cmp_eq_u32_e64 s[2:3], s9, v37
	s_nop 1
	v_cndmask_b32_e64 v37, 0, v100, s[2:3]
	v_cmp_eq_u32_e64 s[2:3], s9, v38
	s_nop 1
	v_cndmask_b32_e64 v38, 0, v44, s[2:3]
	v_cmp_eq_u32_e64 s[2:3], s9, v39
	s_nop 1
	v_cndmask_b32_e64 v39, 0, v44, s[2:3]
	s_waitcnt lgkmcnt(0)
	v_cmp_eq_u32_e64 s[2:3], s9, v40
	v_bfrev_b32_e32 v44, 1
	s_nop 0
	v_cndmask_b32_e64 v40, 0, 2.0, s[2:3]
	v_cmp_eq_u32_e64 s[2:3], s9, v41
	s_nop 1
	v_cndmask_b32_e64 v41, 0, 2.0, s[2:3]
	v_cmp_eq_u32_e64 s[2:3], s9, v42
	s_nop 1
	v_cndmask_b32_e64 v42, 0, v44, s[2:3]
	v_cmp_eq_u32_e64 s[2:3], s9, v43
	s_nop 1
	v_cndmask_b32_e64 v43, 0, v44, s[2:3]
	v_cndmask_b32_e64 v44, 0, 1, s[0:1]
	v_or3_b32 v44, v45, v44, v46
	v_or3_b32 v44, v44, v47, v48
	v_or3_b32 v44, v44, v49, v52
	v_or3_b32 v44, v44, v53, v54
	v_or3_b32 v44, v44, v55, v56
	v_or3_b32 v44, v44, v57, v58
	v_or3_b32 v44, v44, v59, v60
	v_or3_b32 v44, v44, v62, v61
	v_or3_b32 v44, v44, v63, v64
	v_or3_b32 v44, v44, v65, v66
	v_or3_b32 v44, v44, v67, v68
	v_or3_b32 v44, v44, v70, v69
	v_or3_b32 v44, v44, v71, v72
	v_or3_b32 v44, v44, v73, v74
	v_or3_b32 v44, v44, v75, v76
	v_or3_b32 v44, v44, v78, v77
	v_or3_b32 v35, v44, v79, v35
	v_or3_b32 v35, v35, v80, v81
	v_or3_b32 v35, v35, v82, v83
	v_or3_b32 v35, v35, v85, v84
	v_or3_b32 v35, v35, v86, v87
	v_or3_b32 v35, v35, v88, v89
	v_or3_b32 v35, v35, v90, v91
	v_or3_b32 v35, v35, v93, v92
	v_or3_b32 v35, v35, v94, v95
	v_or3_b32 v35, v35, v96, v97
	v_or3_b32 v35, v35, v98, v99
	v_or3_b32 v35, v35, v36, v37
	v_or3_b32 v35, v35, v38, v39
	v_add_u32_e32 v37, -1, v50
	v_or3_b32 v35, v35, v40, v41
	v_cmp_lt_i32_e32 vcc, v37, v51
	v_or3_b32 v35, v35, v42, v43
	v_bcnt_u32_b32 v36, v35, 0
	v_cndmask_b32_e32 v37, v37, v50, vcc
	v_lshlrev_b32_e32 v37, 2, v37
	ds_bpermute_b32 v37, v37, v36
	v_cmp_lt_i32_e32 vcc, 0, v34
	v_add_u32_e32 v38, -2, v50
	v_mov_b32_e32 v39, 0
	s_waitcnt lgkmcnt(0)
	v_cndmask_b32_e32 v37, 0, v37, vcc
	v_cmp_lt_i32_e32 vcc, v38, v51
	v_bcnt_u32_b32 v37, v35, v37
	s_nop 0
	v_cndmask_b32_e32 v38, v38, v50, vcc
	v_lshlrev_b32_e32 v38, 2, v38
	ds_bpermute_b32 v38, v38, v37
	v_cmp_lt_i32_e32 vcc, 1, v34
	s_waitcnt lgkmcnt(0)
	s_nop 0
	v_cndmask_b32_e32 v38, 0, v38, vcc
	v_add_u32_e32 v37, v38, v37
	v_add_u32_e32 v38, -4, v50
	v_cmp_lt_i32_e32 vcc, v38, v51
	s_nop 1
	v_cndmask_b32_e32 v38, v38, v50, vcc
	v_lshlrev_b32_e32 v38, 2, v38
	ds_bpermute_b32 v38, v38, v37
	v_cmp_lt_i32_e32 vcc, 3, v34
	s_waitcnt lgkmcnt(0)
	s_nop 0
	v_cndmask_b32_e32 v38, 0, v38, vcc
	v_add_u32_e32 v37, v38, v37
	v_add_u32_e32 v38, -8, v50
	v_cmp_lt_i32_e32 vcc, v38, v51
	s_nop 1
	v_cndmask_b32_e32 v38, v38, v50, vcc
	v_lshlrev_b32_e32 v38, 2, v38
	ds_bpermute_b32 v38, v38, v37
	v_cmp_lt_i32_e32 vcc, 7, v34
	s_waitcnt lgkmcnt(0)
	s_nop 0
	v_cndmask_b32_e32 v38, 0, v38, vcc
	v_add_u32_e32 v37, v38, v37
	v_add_u32_e32 v38, -16, v50
	v_cmp_lt_i32_e32 vcc, v38, v51
	s_nop 1
	v_cndmask_b32_e32 v38, v38, v50, vcc
	v_lshlrev_b32_e32 v38, 2, v38
	ds_bpermute_b32 v38, v38, v37
	v_cmp_lt_i32_e32 vcc, 15, v34
	s_waitcnt lgkmcnt(0)
	s_nop 0
	v_cndmask_b32_e32 v38, 0, v38, vcc
	v_add_u32_e32 v37, v38, v37
	v_subrev_u32_e32 v38, 32, v50
	v_cmp_lt_i32_e32 vcc, v38, v51
	s_nop 1
	v_cndmask_b32_e32 v38, v38, v50, vcc
	v_lshlrev_b32_e32 v38, 2, v38
	ds_bpermute_b32 v38, v38, v37
	s_cbranch_scc1 .LBB1_73
	s_mov_b32 s0, 0x24800
	v_mov_b32_e32 v39, 0

.LBB1_82:
	v_mov_b32_e32 v52, v0
	v_mov_b32_e32 v36, v0
	s_movk_i32 s0, 0xff80
	v_lshrrev_b32_e32 v34, 1, v36
	v_and_b32_e32 v34, 28, v34
	v_lshlrev_b32_e32 v35, 1, v36
	v_and_or_b32 v34, v35, s0, v34
	v_add_u32_e32 v37, 0x24000, v34
	ds_read2_b32 v[34:35], v37 offset1:8
	v_lshlrev_b32_e32 v36, 3, v36
	s_movk_i32 s22, 0x300
	v_and_b32_e32 v38, 56, v36
	ds_read2_b32 v[36:37], v37 offset0:16 offset1:24
	s_waitcnt lgkmcnt(1)
	v_mul_lo_u32 v34, v34, s22
	v_or_b32_e32 v34, v34, v38
	v_lshlrev_b32_e32 v198, 1, v34
	v_mul_lo_u32 v34, v35, s22
	v_or_b32_e32 v34, v34, v38
	v_lshlrev_b32_e32 v199, 1, v34
	s_waitcnt lgkmcnt(0)
	v_mul_lo_u32 v34, v36, s22
	v_or_b32_e32 v34, v34, v38
	v_lshlrev_b32_e32 v200, 1, v34
	v_mul_lo_u32 v34, v37, s22
	v_or_b32_e32 v34, v34, v38
	v_lshlrev_b32_e32 v201, 1, v34
	v_mov_b32_e32 v34, v198
	v_mov_b32_e32 v38, v199
	global_load_dwordx4 v[34:37], v34, s[80:81]
	v_mov_b32_e32 v42, v200
	global_load_dwordx4 v[38:41], v38, s[80:81]
	v_mov_b32_e32 v46, v201
	global_load_dwordx4 v[42:45], v42, s[80:81]
	global_load_dwordx4 v[46:49], v46, s[80:81]
	global_load_dwordx4 v[146:149], v198, s[80:81] offset:128
	global_load_dwordx4 v[150:153], v199, s[80:81] offset:128
	global_load_dwordx4 v[154:157], v200, s[80:81] offset:128
	global_load_dwordx4 v[158:161], v201, s[80:81] offset:128
	v_lshrrev_b32_e32 v53, 2, v52
	v_and_b32_e32 v53, 0xffffe0, v53
	v_add_u32_e32 v53, s13, v53
	v_lshrrev_b32_e32 v54, 3, v52
	v_and_or_b32 v53, v54, 7, v53
	v_mul_lo_u32 v53, v53, s22
	v_lshlrev_b32_e32 v52, 2, v52
	v_and_or_b32 v52, v52, 28, v53
	v_mov_b32_e32 v53, v0
	s_movk_i32 s0, 0x400
	v_lshlrev_b32_e32 v57, 4, v53
	v_lshlrev_b32_e32 v54, 8, v53
	v_lshlrev_b32_e32 v55, 3, v53
	v_and_b32_e32 v57, 48, v57
	v_lshlrev_b32_e32 v53, 6, v53
	v_and_b32_e32 v56, 0x1c0, v55
	v_and_or_b32 v54, v54, s0, v57
	v_and_b32_e32 v53, 0xfffff000, v53
	v_or3_b32 v57, v54, v56, v53
	s_waitcnt vmcnt(7)
	ds_write_b128 v57, v[34:37]
	v_bitop3_b32 v34, v54, 32, v56 bitop3:0x36
	v_or_b32_e32 v34, v53, v34
	s_waitcnt vmcnt(6)
	ds_write_b128 v34, v[38:41] offset:512
	s_waitcnt vmcnt(5)
	ds_write_b128 v57, v[42:45] offset:2048
	s_waitcnt vmcnt(4)
	ds_write_b128 v34, v[46:49] offset:2560
	v_and_b32_e32 v34, 0x1f8, v55
	v_cvt_pk_f16_f32 v29, v28, v29
	v_cvt_pk_f16_f32 v28, v26, v27
	v_or_b32_e32 v26, v34, v53
	v_cvt_pk_f16_f32 v21, v20, v21
	v_cvt_pk_f16_f32 v20, v18, v19
	ds_write2st64_b64 v26, v[28:29], v[20:21] offset0:64 offset1:66
	v_mov_b32_e32 v20, 0x1f8
	v_cvt_pk_f16_f32 v17, v16, v17
	v_cvt_pk_f16_f32 v16, v14, v15
	v_cvt_pk_f16_f32 v15, v24, v25
	v_cvt_pk_f16_f32 v14, v22, v23
	v_bitop3_b32 v20, v55, 32, v20 bitop3:0x6c
	ds_write_b64 v26, v[14:15] offset:34816
	v_or_b32_e32 v14, 0xc00, v53
	v_cvt_pk_f16_f32 v19, v32, v33
	v_cvt_pk_f16_f32 v18, v30, v31
	v_or_b32_e32 v21, v20, v53
	v_cvt_pk_f16_f32 v9, v8, v9
	v_cvt_pk_f16_f32 v8, v6, v7
	v_or_b32_e32 v6, v34, v14
	s_movk_i32 s0, 0xf800
	ds_write2st64_b64 v21, v[18:19], v[16:17] offset0:65 offset1:67
	ds_write_b64 v6, v[8:9] offset:32768
	v_cvt_pk_f16_f32 v7, v12, v13
	v_cvt_pk_f16_f32 v6, v10, v11
	v_and_or_b32 v8, v14, s0, v20
	v_cvt_pk_f16_f32 v5, v4, v5
	v_cvt_pk_f16_f32 v4, v2, v3
	v_or_b32_e32 v2, v20, v14
	ds_write_b64 v8, v[6:7] offset:33280
	ds_write_b64 v2, v[4:5] offset:33280
	v_lshlrev_b32_e32 v202, 2, v52
	v_mov_b32_e32 v194, v202
	v_mov_b32_e32 v195, 0
	s_movk_i32 s23, 0x6000
	s_mov_b32 s24, 0xc000
	s_mov_b32 s25, 0x12000
	s_waitcnt vmcnt(0)
	v_mov_b32_e32 v2, v146
	v_mov_b32_e32 v3, v147
	v_mov_b32_e32 v4, v148
	v_mov_b32_e32 v5, v149
	v_mov_b32_e32 v6, v150
	v_mov_b32_e32 v7, v151
	v_mov_b32_e32 v8, v152
	v_mov_b32_e32 v9, v153
	v_mov_b32_e32 v10, v154
	v_mov_b32_e32 v11, v155
	v_mov_b32_e32 v12, v156
	v_mov_b32_e32 v13, v157
	v_mov_b32_e32 v14, v158
	v_mov_b32_e32 v15, v159
	v_mov_b32_e32 v16, v160
	v_mov_b32_e32 v17, v161
	v_mov_b32_e32 v22, v114
	v_mov_b32_e32 v23, v115
	v_mov_b32_e32 v24, v116
	v_mov_b32_e32 v25, v117
	v_mov_b32_e32 v18, v118
	v_mov_b32_e32 v19, v119
	v_mov_b32_e32 v20, v120
	v_mov_b32_e32 v21, v121
	v_mov_b32_e32 v30, v122
	v_mov_b32_e32 v31, v123
	v_mov_b32_e32 v32, v124
	v_mov_b32_e32 v33, v125
	v_mov_b32_e32 v26, v126
	v_mov_b32_e32 v27, v127
	v_mov_b32_e32 v28, v128
	v_mov_b32_e32 v29, v129
	v_mov_b32_e32 v38, v130
	v_mov_b32_e32 v39, v131
	v_mov_b32_e32 v40, v132
	v_mov_b32_e32 v41, v133
	v_mov_b32_e32 v34, v134
	v_mov_b32_e32 v35, v135
	v_mov_b32_e32 v36, v136
	v_mov_b32_e32 v37, v137
	v_mov_b32_e32 v46, v138
	v_mov_b32_e32 v47, v139
	v_mov_b32_e32 v48, v140
	v_mov_b32_e32 v49, v141
	v_mov_b32_e32 v42, v142
	v_mov_b32_e32 v43, v143
	v_mov_b32_e32 v44, v144
	v_mov_b32_e32 v45, v145
	s_movk_i32 s26, 0x1f8
	s_mov_b32 s27, 0
	v_add_u32_e32 v52, -1, v50
	v_cmp_lt_i32_e32 vcc, v52, v51
	s_mov_b64 s[10:11], -1
	v_mov_b32_e32 v228, s12
	v_cndmask_b32_e32 v52, v52, v50, vcc
	v_lshlrev_b32_e32 v203, 2, v52
	v_add_u32_e32 v52, -2, v50
	v_cmp_lt_i32_e32 vcc, v52, v51
	s_movk_i32 s28, 0x100
	s_movk_i32 s29, 0x80
	v_cndmask_b32_e32 v52, v52, v50, vcc
	v_lshlrev_b32_e32 v204, 2, v52
	v_add_u32_e32 v52, -4, v50
	v_cmp_lt_i32_e32 vcc, v52, v51
	s_movk_i32 s30, 0x220
	s_mov_b32 s31, 0x5040100
	v_cndmask_b32_e32 v52, v52, v50, vcc
	v_lshlrev_b32_e32 v205, 2, v52
	v_add_u32_e32 v52, -8, v50
	v_cmp_lt_i32_e32 vcc, v52, v51
	s_mov_b32 s33, 0x7060302
	v_mov_b32_e32 v209, 0x20000
	v_cndmask_b32_e32 v52, v52, v50, vcc
	v_lshlrev_b32_e32 v206, 2, v52
	v_add_u32_e32 v52, -16, v50
	v_cmp_lt_i32_e32 vcc, v52, v51
	v_mov_b32_e32 v219, 0x10000
	v_mov_b32_e32 v221, 0x80000
	v_cndmask_b32_e32 v52, v52, v50, vcc
	v_lshlrev_b32_e32 v207, 2, v52
	v_subrev_u32_e32 v52, 32, v50
	v_cmp_lt_i32_e32 vcc, v52, v51
	v_mov_b32_e32 v222, 0x100000
	v_mov_b32_e32 v223, 0x200000
	v_cndmask_b32_e32 v50, v52, v50, vcc
	v_lshlrev_b32_e32 v208, 2, v50
	v_mov_b32_e32 v224, 0x400000
	v_mov_b32_e32 v225, 0x800000
	v_mov_b32_e32 v226, 0x1000000
	v_bfrev_b32_e32 v227, 64
	v_bfrev_b32_e32 v229, 32
	v_bfrev_b32_e32 v230, 16
	v_bfrev_b32_e32 v231, 8
	v_bfrev_b32_e32 v232, 4
	v_bfrev_b32_e32 v233, 1
	s_waitcnt lgkmcnt(0)
	s_barrier
	s_branch .LBB1_84

.LBB1_117:
	s_cmp_lt_u32 s37, 10
	s_cselect_b32 s12, 2, -10
	s_add_i32 s12, s12, s37
	s_add_i32 s12, s12, s77
	s_cmp_ge_u32 s12, 12
	s_cselect_b32 s13, 12, 0
	s_sub_i32 s12, s12, s13
	s_lshl_b32 s13, s12, 7
	s_add_u32 s14, s13, s52
	s_addc_u32 s15, 0, s53
	s_lshl_b32 s12, s12, 8
	s_add_u32 s12, s8, s12
	s_addc_u32 s13, s9, 0
	s_and_b32 s38, s36, 0x10000
	s_xor_b32 s39, s38, 0x10000
	v_or_b32_e32 v210, s38, v237
	v_mov_b32_e32 v194, v202
	v_add_u32_e32 v196, s39, v239
	v_add_u32_e32 v197, s39, v240
	v_add_u32_e32 v216, s39, v241
	v_add_u32_e32 v217, s39, v242
	v_or_b32_e32 v218, s38, v238
	v_add_u32_e32 v220, v210, v236
	ds_read_b128 v[186:189], v218 offset:32768
	ds_read_b128 v[190:193], v218 offset:34816
	ds_read_b128 v[182:185], v218 offset:36864
	ds_read_b128 v[178:181], v218 offset:38912
	ds_read_b128 v[244:247], v220
	ds_read_b128 v[248:251], v220 offset:2048
	ds_read_b128 v[252:255], v220 offset:4096
	ds_read_b128 v[210:213], v220 offset:6144
	s_waitcnt lgkmcnt(3)
	v_mfma_f32_16x16x32_f16 v[170:173], v[244:247], v[186:189], v[170:173]
	v_mfma_f32_16x16x32_f16 v[162:165], v[244:247], v[190:193], v[162:165]
	v_mfma_f32_16x16x32_f16 v[174:177], v[244:247], v[182:185], v[174:177]
	v_mfma_f32_16x16x32_f16 v[166:169], v[244:247], v[178:181], v[166:169]
	ds_read_b128 v[244:247], v220 offset:8192
	s_waitcnt vmcnt(8)
	ds_write_b128 v196, v[2:5]
	global_load_dwordx4 v[2:5], v198, s[14:15]
	s_waitcnt lgkmcnt(4)
	v_mfma_f32_16x16x32_f16 v[154:157], v[248:251], v[186:189], v[154:157]
	v_mfma_f32_16x16x32_f16 v[146:149], v[248:251], v[190:193], v[146:149]
	v_mfma_f32_16x16x32_f16 v[158:161], v[248:251], v[182:185], v[158:161]
	v_mfma_f32_16x16x32_f16 v[150:153], v[248:251], v[178:181], v[150:153]
	ds_read_b128 v[248:251], v220 offset:10240
	ds_write_b128 v197, v[6:9]
	global_load_dwordx4 v[6:9], v199, s[14:15]
	s_waitcnt lgkmcnt(5)
	v_mfma_f32_16x16x32_f16 v[138:141], v[252:255], v[186:189], v[138:141]
	v_mfma_f32_16x16x32_f16 v[130:133], v[252:255], v[190:193], v[130:133]
	v_mfma_f32_16x16x32_f16 v[142:145], v[252:255], v[182:185], v[142:145]
	v_mfma_f32_16x16x32_f16 v[134:137], v[252:255], v[178:181], v[134:137]
	ds_read_b128 v[252:255], v220 offset:12288
	ds_write_b128 v196, v[10:13] offset:2048
	global_load_dwordx4 v[10:13], v200, s[14:15]
	s_waitcnt lgkmcnt(6)
	v_mfma_f32_16x16x32_f16 v[122:125], v[210:213], v[186:189], v[122:125]
	v_mfma_f32_16x16x32_f16 v[114:117], v[210:213], v[190:193], v[114:117]
	v_mfma_f32_16x16x32_f16 v[126:129], v[210:213], v[182:185], v[126:129]
	v_mfma_f32_16x16x32_f16 v[118:121], v[210:213], v[178:181], v[118:121]
	ds_read_b128 v[210:213], v220 offset:14336
	ds_write_b128 v197, v[14:17] offset:2048
	global_load_dwordx4 v[14:17], v201, s[14:15]
	s_waitcnt lgkmcnt(7)
	v_mfma_f32_16x16x32_f16 v[106:109], v[244:247], v[186:189], v[106:109]
	v_lshl_add_u64 v[196:197], s[12:13], 0, v[194:195]
	v_mfma_f32_16x16x32_f16 v[98:101], v[244:247], v[190:193], v[98:101]
	v_mfma_f32_16x16x32_f16 v[110:113], v[244:247], v[182:185], v[110:113]
	v_mfma_f32_16x16x32_f16 v[102:105], v[244:247], v[178:181], v[102:105]
	ds_read_b128 v[244:247], v220 offset:1024
	s_waitcnt vmcnt(11)
	v_cvt_pk_f16_f32 v25, v24, v25
	v_cvt_pk_f16_f32 v24, v22, v23
	ds_write_b64 v216, v[24:25]
	global_load_dwordx4 v[22:25], v194, s[12:13] nt
	s_waitcnt lgkmcnt(7)
	v_mfma_f32_16x16x32_f16 v[90:93], v[248:251], v[186:189], v[90:93]
	v_mfma_f32_16x16x32_f16 v[82:85], v[248:251], v[190:193], v[82:85]
	v_mfma_f32_16x16x32_f16 v[94:97], v[248:251], v[182:185], v[94:97]
	v_mfma_f32_16x16x32_f16 v[86:89], v[248:251], v[178:181], v[86:89]
	ds_read_b128 v[248:251], v220 offset:3072
	s_waitcnt vmcnt(11)
	v_cvt_pk_f16_f32 v21, v20, v21
	v_cvt_pk_f16_f32 v20, v18, v19
	ds_write_b64 v216, v[20:21] offset:1024
	global_load_dwordx4 v[18:21], v194, s[12:13] offset:128 nt
	s_waitcnt lgkmcnt(7)
	v_mfma_f32_16x16x32_f16 v[74:77], v[252:255], v[186:189], v[74:77]
	v_add_co_u32_e32 v214, vcc, s23, v196
	v_mfma_f32_16x16x32_f16 v[66:69], v[252:255], v[190:193], v[66:69]
	s_nop 0
	v_addc_co_u32_e32 v215, vcc, 0, v197, vcc
	v_mfma_f32_16x16x32_f16 v[78:81], v[252:255], v[182:185], v[78:81]
	v_mfma_f32_16x16x32_f16 v[70:73], v[252:255], v[178:181], v[70:73]
	ds_read_b128 v[252:255], v220 offset:5120
	s_waitcnt vmcnt(11)
	v_cvt_pk_f16_f32 v33, v32, v33
	v_cvt_pk_f16_f32 v32, v30, v31
	ds_write_b64 v217, v[32:33]
	global_load_dwordx4 v[30:33], v[214:215], off nt
	s_waitcnt lgkmcnt(7)
	v_mfma_f32_16x16x32_f16 v[62:65], v[210:213], v[186:189], v[62:65]
	ds_read_b128 v[186:189], v220 offset:7168
	s_waitcnt vmcnt(11)
	v_mfma_f32_16x16x32_f16 v[58:61], v[210:213], v[182:185], v[58:61]
	v_cvt_pk_f16_f32 v183, v28, v29
	v_cvt_pk_f16_f32 v182, v26, v27
	global_load_dwordx4 v[26:29], v[214:215], off offset:128 nt
	v_mfma_f32_16x16x32_f16 v[54:57], v[210:213], v[190:193], v[54:57]
	ds_write_b64 v217, v[182:183] offset:1024
	v_mfma_f32_16x16x32_f16 v[50:53], v[210:213], v[178:181], v[50:53]
	ds_read_b128 v[178:181], v218 offset:33792
	ds_read_b128 v[182:185], v218 offset:35840
	ds_read_b128 v[190:193], v218 offset:37888
	ds_read_b128 v[210:213], v218 offset:39936
	s_waitcnt lgkmcnt(0)
	v_mfma_f32_16x16x32_f16 v[170:173], v[244:247], v[178:181], v[170:173]
	v_add_co_u32_e32 v214, vcc, s24, v196
	v_mfma_f32_16x16x32_f16 v[162:165], v[244:247], v[182:185], v[162:165]
	v_addc_co_u32_e32 v215, vcc, 0, v197, vcc
	v_mfma_f32_16x16x32_f16 v[174:177], v[244:247], v[190:193], v[174:177]
	v_mfma_f32_16x16x32_f16 v[166:169], v[244:247], v[210:213], v[166:169]
	ds_read_b128 v[244:247], v220 offset:9216
	s_waitcnt vmcnt(11)
	v_cvt_pk_f16_f32 v41, v40, v41
	v_cvt_pk_f16_f32 v40, v38, v39
	ds_write_b64 v216, v[40:41] offset:2048
	global_load_dwordx4 v[38:41], v[214:215], off nt
	v_mfma_f32_16x16x32_f16 v[154:157], v[248:251], v[178:181], v[154:157]
	v_mfma_f32_16x16x32_f16 v[146:149], v[248:251], v[182:185], v[146:149]
	v_mfma_f32_16x16x32_f16 v[158:161], v[248:251], v[190:193], v[158:161]
	v_mfma_f32_16x16x32_f16 v[150:153], v[248:251], v[210:213], v[150:153]
	ds_read_b128 v[248:251], v220 offset:11264
	s_waitcnt vmcnt(11)
	v_cvt_pk_f16_f32 v37, v36, v37
	v_cvt_pk_f16_f32 v36, v34, v35
	ds_write_b64 v216, v[36:37] offset:3072
	global_load_dwordx4 v[34:37], v[214:215], off offset:128 nt
	v_mfma_f32_16x16x32_f16 v[138:141], v[252:255], v[178:181], v[138:141]
	v_add_co_u32_e32 v196, vcc, s25, v196
	v_mfma_f32_16x16x32_f16 v[130:133], v[252:255], v[182:185], v[130:133]
	s_nop 0
	v_addc_co_u32_e32 v197, vcc, 0, v197, vcc
	v_mfma_f32_16x16x32_f16 v[142:145], v[252:255], v[190:193], v[142:145]
	v_mfma_f32_16x16x32_f16 v[134:137], v[252:255], v[210:213], v[134:137]
	ds_read_b128 v[252:255], v220 offset:13312
	s_waitcnt vmcnt(11)
	v_cvt_pk_f16_f32 v49, v48, v49
	v_cvt_pk_f16_f32 v48, v46, v47
	ds_write_b64 v217, v[48:49] offset:2048
	global_load_dwordx4 v[46:49], v[196:197], off nt
	v_mfma_f32_16x16x32_f16 v[122:125], v[186:189], v[178:181], v[122:125]
	v_mfma_f32_16x16x32_f16 v[114:117], v[186:189], v[182:185], v[114:117]
	v_mfma_f32_16x16x32_f16 v[126:129], v[186:189], v[190:193], v[126:129]
	v_mfma_f32_16x16x32_f16 v[118:121], v[186:189], v[210:213], v[118:121]
	ds_read_b128 v[186:189], v220 offset:15360
	s_waitcnt vmcnt(11)
	v_cvt_pk_f16_f32 v45, v44, v45
	v_cvt_pk_f16_f32 v44, v42, v43
	ds_write_b64 v217, v[44:45] offset:3072
	global_load_dwordx4 v[42:45], v[196:197], off offset:128 nt
	s_waitcnt lgkmcnt(7)
	v_mfma_f32_16x16x32_f16 v[106:109], v[244:247], v[178:181], v[106:109]
	v_mfma_f32_16x16x32_f16 v[98:101], v[244:247], v[182:185], v[98:101]
	v_mfma_f32_16x16x32_f16 v[110:113], v[244:247], v[190:193], v[110:113]
	v_mfma_f32_16x16x32_f16 v[102:105], v[244:247], v[210:213], v[102:105]
	s_waitcnt lgkmcnt(5)
	v_mfma_f32_16x16x32_f16 v[90:93], v[248:251], v[178:181], v[90:93]
	v_mfma_f32_16x16x32_f16 v[82:85], v[248:251], v[182:185], v[82:85]
	v_mfma_f32_16x16x32_f16 v[94:97], v[248:251], v[190:193], v[94:97]
	v_mfma_f32_16x16x32_f16 v[86:89], v[248:251], v[210:213], v[86:89]
	s_waitcnt lgkmcnt(3)
	v_mfma_f32_16x16x32_f16 v[74:77], v[252:255], v[178:181], v[74:77]
	v_mfma_f32_16x16x32_f16 v[66:69], v[252:255], v[182:185], v[66:69]
	v_mfma_f32_16x16x32_f16 v[78:81], v[252:255], v[190:193], v[78:81]
	v_mfma_f32_16x16x32_f16 v[70:73], v[252:255], v[210:213], v[70:73]
	s_waitcnt lgkmcnt(1)
	v_mfma_f32_16x16x32_f16 v[62:65], v[186:189], v[178:181], v[62:65]
	v_mfma_f32_16x16x32_f16 v[54:57], v[186:189], v[182:185], v[54:57]
	v_mfma_f32_16x16x32_f16 v[58:61], v[186:189], v[190:193], v[58:61]
	v_mfma_f32_16x16x32_f16 v[50:53], v[186:189], v[210:213], v[50:53]
	s_add_i32 s37, s37, 1
	s_add_i32 s36, s36, 0x10000
	s_cmp_eq_u32 s36, 0xc0000
	s_waitcnt lgkmcnt(0)
	s_barrier
	s_cbranch_scc1 .LBB1_83
.LBB1_118:
	s_cmp_lg_u32 s36, 0xa0000
	s_cselect_b64 s[12:13], -1, 0
	s_or_b64 s[12:13], s[2:3], s[12:13]
	s_and_b64 vcc, exec, s[12:13]
	s_cbranch_vccnz .LBB1_117
	v_mov_b32_e32 v180, v0
	v_mov_b32_e32 v182, v0
	v_lshrrev_b32_e32 v178, 2, v180
	v_and_b32_e32 v178, 0xffffe0, v178
	v_add_u32_e32 v178, s35, v178
	v_lshrrev_b32_e32 v179, 3, v180
	v_and_or_b32 v178, v179, 7, v178
	v_mul_lo_u32 v181, v178, s22
	v_lshlrev_b32_e32 v180, 2, v180
	v_lshrrev_b32_e32 v178, 1, v182
	v_lshlrev_b32_e32 v179, 1, v182
	v_and_b32_e32 v178, 28, v178
	v_and_b32_e32 v179, 0xffffff80, v179
	v_add3_u32 v183, v243, v178, v179
	ds_read2_b32 v[178:179], v183 offset1:8
	v_and_or_b32 v184, v180, 28, v181
	v_lshlrev_b32_e32 v180, 3, v182
	v_and_b32_e32 v182, 56, v180
	ds_read2_b32 v[180:181], v183 offset0:16 offset1:24
	s_waitcnt lgkmcnt(1)
	v_mul_lo_u32 v178, v178, s22
	v_or_b32_e32 v178, v178, v182
	v_lshlrev_b32_e32 v198, 1, v178
	v_mul_lo_u32 v178, v179, s22
	v_or_b32_e32 v178, v178, v182
	v_lshlrev_b32_e32 v199, 1, v178
	s_waitcnt lgkmcnt(0)
	v_mul_lo_u32 v178, v180, s22
	v_or_b32_e32 v178, v178, v182
	v_lshlrev_b32_e32 v200, 1, v178
	v_mul_lo_u32 v178, v181, s22
	v_or_b32_e32 v178, v178, v182
	v_lshlrev_b32_e32 v201, 1, v178
	v_lshlrev_b32_e32 v202, 2, v184
	s_mov_b32 s16, s17
	s_lshr_b32 s82, s35, 7
	s_and_b32 s77, s82, 7
	v_mov_b32_e32 v234, v235
	s_mov_b64 s[8:9], s[0:1]
	s_branch .LBB1_117
